# code placement: L0 attention loop moved to the same byte phase as L1 (24 mod 64); later code phase unchanged
# baseline (speedup 1.0000x reference)
.LBB0_259:
	s_add_i32 s21, s21, 1
	s_cmp_eq_u32 s21, 4
	s_cbranch_scc1 .LBB0_349
	s_nop 0
	s_nop 0

.LBB0_346:
	v_max_f32_e32 v16, v16, v16
	v_max_f32_e32 v17, 0, v16
	v_exp_f32_e64 v16, -v17
	v_cmp_gt_u32_e32 vcc, 32, v230
	s_and_saveexec_b64 s[2:3], vcc
	ds_write_b32 v235, v16
	s_or_b64 exec, exec, s[2:3]
	v_sub_f32_e32 v113, v113, v17
	v_sub_f32_e32 v112, v112, v17
	v_sub_f32_e32 v111, v111, v17
	v_sub_f32_e32 v110, v110, v17
	v_sub_f32_e32 v109, v109, v17
	v_sub_f32_e32 v108, v108, v17
	v_sub_f32_e32 v107, v107, v17
	v_sub_f32_e32 v106, v106, v17
	v_sub_f32_e32 v105, v105, v17
	v_sub_f32_e32 v104, v104, v17
	v_sub_f32_e32 v103, v103, v17
	v_sub_f32_e32 v102, v102, v17
	v_sub_f32_e32 v101, v101, v17
	v_sub_f32_e32 v100, v100, v17
	v_sub_f32_e32 v99, v99, v17
	v_sub_f32_e32 v98, v98, v17
	v_sub_f32_e32 v97, v97, v17
	v_sub_f32_e32 v96, v96, v17
	v_sub_f32_e32 v95, v95, v17
	v_sub_f32_e32 v94, v94, v17
	v_sub_f32_e32 v93, v93, v17
	v_sub_f32_e32 v92, v92, v17
	v_sub_f32_e32 v91, v91, v17
	v_sub_f32_e32 v90, v90, v17
	v_sub_f32_e32 v89, v89, v17
	v_sub_f32_e32 v88, v88, v17
	v_sub_f32_e32 v87, v87, v17
	v_sub_f32_e32 v86, v86, v17
	v_sub_f32_e32 v85, v85, v17
	v_sub_f32_e32 v84, v84, v17
	v_sub_f32_e32 v83, v83, v17
	v_sub_f32_e32 v82, v82, v17
	v_mul_f32_e32 v243, v243, v16
	s_branch .LBB0_340
	s_nop 0
	s_nop 0
	s_nop 0
	s_nop 0
	s_nop 0
	s_nop 0
	s_nop 0
	s_nop 0
	s_nop 0
	s_nop 0
	s_nop 0
	s_nop 0
	s_nop 0
	s_nop 0
